# kswz-repeat: K-tile LDS 4-bit swizzle, second paired measurement
# baseline (speedup 1.0000x reference)
.LBB0_3491:
	s_add_i32 s50, s50, 1
	v_readlane_b32 s14, v252, 52
	s_mul_i32 s16, s50, s14
	s_add_i32 s16, s16, s88
	v_readlane_b32 s15, v252, 53
	s_cmpk_lt_i32 s16, 0x800
	s_cselect_b64 s[14:15], -1, 0
	s_cmpk_gt_i32 s16, 0x7ff
	s_cbranch_scc1 .LBB0_3493
	s_and_b32 s16, s16, 0x1ff
	s_ashr_i32 s19, s16, 5
	s_and_b32 s17, s16, 7
	s_and_b32 s19, s19, -8
	s_or_b32 s17, s19, s17
	s_and_b32 s20, s16, 48
	s_add_i32 s20, s17, s20
	s_bfe_u32 s19, s16, 0x20006
	s_lshl_b32 s20, s20, 1
	s_bfe_u32 s16, s16, 0x10003
	s_or_b32 s51, s20, s16
	s_lshl_b32 s16, s17, 2
	s_or_b32 s52, s16, s19

.LBB0_3497:
	v_mov_b32_e32 v127, 0
	s_andn2_b64 vcc, exec, s[10:11]
	v_mov_b32_e32 v126, v127
	v_mov_b32_e32 v125, v127
	v_mov_b32_e32 v124, v127
	v_mov_b32_e32 v131, v127
	v_mov_b32_e32 v130, v127
	v_mov_b32_e32 v129, v127
	v_mov_b32_e32 v128, v127
	v_mov_b32_e32 v115, v127
	v_mov_b32_e32 v114, v127
	v_mov_b32_e32 v113, v127
	v_mov_b32_e32 v112, v127
	v_mov_b32_e32 v111, v127
	v_mov_b32_e32 v110, v127
	v_mov_b32_e32 v109, v127
	v_mov_b32_e32 v108, v127
	v_mov_b32_e32 v99, v127
	v_mov_b32_e32 v98, v127
	v_mov_b32_e32 v97, v127
	v_mov_b32_e32 v96, v127
	v_mov_b32_e32 v95, v127
	v_mov_b32_e32 v94, v127
	v_mov_b32_e32 v93, v127
	v_mov_b32_e32 v92, v127
	v_mov_b32_e32 v83, v127
	v_mov_b32_e32 v82, v127
	v_mov_b32_e32 v81, v127
	v_mov_b32_e32 v80, v127
	v_mov_b32_e32 v79, v127
	v_mov_b32_e32 v78, v127
	v_mov_b32_e32 v77, v127
	v_mov_b32_e32 v76, v127
	v_mov_b32_e32 v123, v127
	v_mov_b32_e32 v122, v127
	v_mov_b32_e32 v121, v127
	v_mov_b32_e32 v120, v127
	v_mov_b32_e32 v119, v127
	v_mov_b32_e32 v118, v127
	v_mov_b32_e32 v117, v127
	v_mov_b32_e32 v116, v127
	v_mov_b32_e32 v107, v127
	v_mov_b32_e32 v106, v127
	v_mov_b32_e32 v105, v127
	v_mov_b32_e32 v104, v127
	v_mov_b32_e32 v103, v127
	v_mov_b32_e32 v102, v127
	v_mov_b32_e32 v101, v127
	v_mov_b32_e32 v100, v127
	v_mov_b32_e32 v91, v127
	v_mov_b32_e32 v90, v127
	v_mov_b32_e32 v89, v127
	v_mov_b32_e32 v88, v127
	v_mov_b32_e32 v87, v127
	v_mov_b32_e32 v86, v127
	v_mov_b32_e32 v85, v127
	v_mov_b32_e32 v84, v127
	v_mov_b32_e32 v75, v127
	v_mov_b32_e32 v74, v127
	v_mov_b32_e32 v73, v127
	v_mov_b32_e32 v72, v127
	v_mov_b32_e32 v71, v127
	v_mov_b32_e32 v70, v127
	v_mov_b32_e32 v69, v127
	v_mov_b32_e32 v68, v127
	v_mov_b32_e32 v67, v127
	v_mov_b32_e32 v66, v127
	v_mov_b32_e32 v65, v127
	v_mov_b32_e32 v64, v127
	v_mov_b32_e32 v63, v127
	v_mov_b32_e32 v62, v127
	v_mov_b32_e32 v61, v127
	v_mov_b32_e32 v60, v127
	v_mov_b32_e32 v51, v127
	v_mov_b32_e32 v50, v127
	v_mov_b32_e32 v49, v127
	v_mov_b32_e32 v48, v127
	v_mov_b32_e32 v47, v127
	v_mov_b32_e32 v46, v127
	v_mov_b32_e32 v45, v127
	v_mov_b32_e32 v44, v127
	v_mov_b32_e32 v35, v127
	v_mov_b32_e32 v34, v127
	v_mov_b32_e32 v33, v127
	v_mov_b32_e32 v32, v127
	v_mov_b32_e32 v31, v127
	v_mov_b32_e32 v30, v127
	v_mov_b32_e32 v29, v127
	v_mov_b32_e32 v28, v127
	v_mov_b32_e32 v19, v127
	v_mov_b32_e32 v18, v127
	v_mov_b32_e32 v17, v127
	v_mov_b32_e32 v16, v127
	v_mov_b32_e32 v15, v127
	v_mov_b32_e32 v14, v127
	v_mov_b32_e32 v13, v127
	v_mov_b32_e32 v12, v127
	v_mov_b32_e32 v59, v127
	v_mov_b32_e32 v58, v127
	v_mov_b32_e32 v57, v127
	v_mov_b32_e32 v56, v127
	v_mov_b32_e32 v55, v127
	v_mov_b32_e32 v54, v127
	v_mov_b32_e32 v53, v127
	v_mov_b32_e32 v52, v127
	v_mov_b32_e32 v43, v127
	v_mov_b32_e32 v42, v127
	v_mov_b32_e32 v41, v127
	v_mov_b32_e32 v40, v127
	v_mov_b32_e32 v39, v127
	v_mov_b32_e32 v38, v127
	v_mov_b32_e32 v37, v127
	v_mov_b32_e32 v36, v127
	v_mov_b32_e32 v27, v127
	v_mov_b32_e32 v26, v127
	v_mov_b32_e32 v25, v127
	v_mov_b32_e32 v24, v127
	v_mov_b32_e32 v23, v127
	v_mov_b32_e32 v22, v127
	v_mov_b32_e32 v21, v127
	v_mov_b32_e32 v20, v127
	v_mov_b32_e32 v11, v127
	v_mov_b32_e32 v10, v127
	v_mov_b32_e32 v9, v127
	v_mov_b32_e32 v8, v127
	v_mov_b32_e32 v7, v127
	v_mov_b32_e32 v6, v127
	v_mov_b32_e32 v5, v127
	v_mov_b32_e32 v4, v127
	s_cbranch_vccnz .LBB0_3500
	s_add_u32 s26, s26, 0x80
	s_addc_u32 s27, s27, 0
	s_add_u32 s19, s30, 0x100
	v_mov_b32_e32 v4, 0
	s_addc_u32 s20, s31, 0
	s_mov_b32 s21, 0
	v_mov_b32_e32 v5, v4
	v_mov_b32_e32 v6, v4
	v_mov_b32_e32 v7, v4
	v_mov_b32_e32 v8, v4
	v_mov_b32_e32 v9, v4
	v_mov_b32_e32 v10, v4
	v_mov_b32_e32 v11, v4
	v_mov_b32_e32 v20, v4
	v_mov_b32_e32 v21, v4
	v_mov_b32_e32 v22, v4
	v_mov_b32_e32 v23, v4
	v_mov_b32_e32 v24, v4
	v_mov_b32_e32 v25, v4
	v_mov_b32_e32 v26, v4
	v_mov_b32_e32 v27, v4
	v_mov_b32_e32 v36, v4
	v_mov_b32_e32 v37, v4
	v_mov_b32_e32 v38, v4
	v_mov_b32_e32 v39, v4
	v_mov_b32_e32 v40, v4
	v_mov_b32_e32 v41, v4
	v_mov_b32_e32 v42, v4
	v_mov_b32_e32 v43, v4
	v_mov_b32_e32 v52, v4
	v_mov_b32_e32 v53, v4
	v_mov_b32_e32 v54, v4
	v_mov_b32_e32 v55, v4
	v_mov_b32_e32 v56, v4
	v_mov_b32_e32 v57, v4
	v_mov_b32_e32 v58, v4
	v_mov_b32_e32 v59, v4
	v_mov_b32_e32 v12, v4
	v_mov_b32_e32 v13, v4
	v_mov_b32_e32 v14, v4
	v_mov_b32_e32 v15, v4
	v_mov_b32_e32 v16, v4
	v_mov_b32_e32 v17, v4
	v_mov_b32_e32 v18, v4
	v_mov_b32_e32 v19, v4
	v_mov_b32_e32 v28, v4
	v_mov_b32_e32 v29, v4
	v_mov_b32_e32 v30, v4
	v_mov_b32_e32 v31, v4
	v_mov_b32_e32 v32, v4
	v_mov_b32_e32 v33, v4
	v_mov_b32_e32 v34, v4
	v_mov_b32_e32 v35, v4
	v_mov_b32_e32 v44, v4
	v_mov_b32_e32 v45, v4
	v_mov_b32_e32 v46, v4
	v_mov_b32_e32 v47, v4
	v_mov_b32_e32 v48, v4
	v_mov_b32_e32 v49, v4
	v_mov_b32_e32 v50, v4
	v_mov_b32_e32 v51, v4
	v_mov_b32_e32 v60, v4
	v_mov_b32_e32 v61, v4
	v_mov_b32_e32 v62, v4
	v_mov_b32_e32 v63, v4
	v_mov_b32_e32 v64, v4
	v_mov_b32_e32 v65, v4
	v_mov_b32_e32 v66, v4
	v_mov_b32_e32 v67, v4
	v_mov_b32_e32 v68, v4
	v_mov_b32_e32 v69, v4
	v_mov_b32_e32 v70, v4
	v_mov_b32_e32 v71, v4
	v_mov_b32_e32 v72, v4
	v_mov_b32_e32 v73, v4
	v_mov_b32_e32 v74, v4
	v_mov_b32_e32 v75, v4
	v_mov_b32_e32 v84, v4
	v_mov_b32_e32 v85, v4
	v_mov_b32_e32 v86, v4
	v_mov_b32_e32 v87, v4
	v_mov_b32_e32 v88, v4
	v_mov_b32_e32 v89, v4
	v_mov_b32_e32 v90, v4
	v_mov_b32_e32 v91, v4
	v_mov_b32_e32 v100, v4
	v_mov_b32_e32 v101, v4
	v_mov_b32_e32 v102, v4
	v_mov_b32_e32 v103, v4
	v_mov_b32_e32 v104, v4
	v_mov_b32_e32 v105, v4
	v_mov_b32_e32 v106, v4
	v_mov_b32_e32 v107, v4
	v_mov_b32_e32 v116, v4
	v_mov_b32_e32 v117, v4
	v_mov_b32_e32 v118, v4
	v_mov_b32_e32 v119, v4
	v_mov_b32_e32 v120, v4
	v_mov_b32_e32 v121, v4
	v_mov_b32_e32 v122, v4
	v_mov_b32_e32 v123, v4
	v_mov_b32_e32 v76, v4
	v_mov_b32_e32 v77, v4
	v_mov_b32_e32 v78, v4
	v_mov_b32_e32 v79, v4
	v_mov_b32_e32 v80, v4
	v_mov_b32_e32 v81, v4
	v_mov_b32_e32 v82, v4
	v_mov_b32_e32 v83, v4
	v_mov_b32_e32 v92, v4
	v_mov_b32_e32 v93, v4
	v_mov_b32_e32 v94, v4
	v_mov_b32_e32 v95, v4
	v_mov_b32_e32 v96, v4
	v_mov_b32_e32 v97, v4
	v_mov_b32_e32 v98, v4
	v_mov_b32_e32 v99, v4
	v_mov_b32_e32 v108, v4
	v_mov_b32_e32 v109, v4
	v_mov_b32_e32 v110, v4
	v_mov_b32_e32 v111, v4
	v_mov_b32_e32 v112, v4
	v_mov_b32_e32 v113, v4
	v_mov_b32_e32 v114, v4
	v_mov_b32_e32 v115, v4
	v_mov_b32_e32 v128, v4
	v_mov_b32_e32 v129, v4
	v_mov_b32_e32 v130, v4
	v_mov_b32_e32 v131, v4
	v_mov_b32_e32 v124, v4
	v_mov_b32_e32 v125, v4
	v_mov_b32_e32 v126, v4
	v_mov_b32_e32 v127, v4
	v_add_u32_e32 v226, 0x10000, v145
.LBB0_3499:
	s_add_i32 s22, s21, 2
	s_add_u32 s23, s26, 0x80
	s_addc_u32 s28, s27, 0
	s_add_i32 s55, 0, 0x10000
	s_cmp_eq_u32 s49, s21
	s_cselect_b32 s31, s15, s28
	s_cselect_b32 s30, s14, s23
	s_cselect_b32 s29, s17, s20
	s_cselect_b32 s28, s16, s19
	s_add_i32 s21, 0, 0x14000
	ds_read_b128 v[148:151], v226
	ds_read_b128 v[152:155], v226 offset:1024
	ds_read_b128 v[156:159], v226 offset:2048
	ds_read_b128 v[160:163], v226 offset:3072
	ds_read_b128 v[164:167], v226 offset:16384
	ds_read_b128 v[168:171], v226 offset:17408
	ds_read_b128 v[172:175], v226 offset:18432
	ds_read_b128 v[176:179], v226 offset:19456
	ds_read_b128 v[180:183], v147
	ds_read_b128 v[184:187], v147 offset:1024
	ds_read_b128 v[188:191], v147 offset:2048
	ds_read_b128 v[192:195], v147 offset:3072
	ds_read_b128 v[196:199], v147 offset:4096
	ds_read_b128 v[200:203], v147 offset:5120
	ds_read_b128 v[204:207], v147 offset:6144
	ds_read_b128 v[208:211], v147 offset:7168
	s_waitcnt vmcnt(6)
	s_waitcnt lgkmcnt(0)
	s_barrier
	s_setprio 1
	s_waitcnt lgkmcnt(0)
	v_mfma_f32_16x16x32_bf16 v[124:127], v[148:151], v[180:183], v[124:127]
	v_mfma_f32_16x16x32_bf16 v[128:131], v[156:159], v[180:183], v[128:131]
	v_mfma_f32_16x16x32_bf16 v[112:115], v[148:151], v[188:191], v[112:115]
	v_mfma_f32_16x16x32_bf16 v[108:111], v[156:159], v[188:191], v[108:111]
	s_add_i32 m0, s42, 0xc000
	s_nop 0
	global_load_lds_dwordx4 v140, s[26:27]
	v_mfma_f32_16x16x32_bf16 v[96:99], v[148:151], v[196:199], v[96:99]
	v_mfma_f32_16x16x32_bf16 v[92:95], v[156:159], v[196:199], v[92:95]
	v_mfma_f32_16x16x32_bf16 v[80:83], v[148:151], v[204:207], v[80:83]
	v_mfma_f32_16x16x32_bf16 v[76:79], v[156:159], v[204:207], v[76:79]
	s_add_i32 m0, s42, 0xe000
	s_nop 0
	global_load_lds_dwordx4 v142, s[26:27]
	v_mfma_f32_16x16x32_bf16 v[124:127], v[152:155], v[184:187], v[124:127]
	v_mfma_f32_16x16x32_bf16 v[128:131], v[160:163], v[184:187], v[128:131]
	v_mfma_f32_16x16x32_bf16 v[112:115], v[152:155], v[192:195], v[112:115]
	v_mfma_f32_16x16x32_bf16 v[108:111], v[160:163], v[192:195], v[108:111]
	v_mfma_f32_16x16x32_bf16 v[96:99], v[152:155], v[200:203], v[96:99]
	v_mfma_f32_16x16x32_bf16 v[92:95], v[160:163], v[200:203], v[92:95]
	v_mfma_f32_16x16x32_bf16 v[80:83], v[152:155], v[208:211], v[80:83]
	v_mfma_f32_16x16x32_bf16 v[76:79], v[160:163], v[208:211], v[76:79]
	s_setprio 0
	s_setprio 1
	v_mfma_f32_16x16x32_bf16 v[120:123], v[164:167], v[180:183], v[120:123]
	v_mfma_f32_16x16x32_bf16 v[116:119], v[172:175], v[180:183], v[116:119]
	v_mfma_f32_16x16x32_bf16 v[104:107], v[164:167], v[188:191], v[104:107]
	v_mfma_f32_16x16x32_bf16 v[100:103], v[172:175], v[188:191], v[100:103]
	v_mfma_f32_16x16x32_bf16 v[88:91], v[164:167], v[196:199], v[88:91]
	v_mfma_f32_16x16x32_bf16 v[84:87], v[172:175], v[196:199], v[84:87]
	v_mfma_f32_16x16x32_bf16 v[72:75], v[164:167], v[204:207], v[72:75]
	v_mfma_f32_16x16x32_bf16 v[68:71], v[172:175], v[204:207], v[68:71]
	v_mfma_f32_16x16x32_bf16 v[120:123], v[168:171], v[184:187], v[120:123]
	v_mfma_f32_16x16x32_bf16 v[116:119], v[176:179], v[184:187], v[116:119]
	v_mfma_f32_16x16x32_bf16 v[104:107], v[168:171], v[192:195], v[104:107]
	v_mfma_f32_16x16x32_bf16 v[100:103], v[176:179], v[192:195], v[100:103]
	v_mfma_f32_16x16x32_bf16 v[88:91], v[168:171], v[200:203], v[88:91]
	v_mfma_f32_16x16x32_bf16 v[84:87], v[176:179], v[200:203], v[84:87]
	v_mfma_f32_16x16x32_bf16 v[72:75], v[168:171], v[208:211], v[72:75]
	v_mfma_f32_16x16x32_bf16 v[68:71], v[176:179], v[208:211], v[68:71]
	s_setprio 0
	s_barrier
	s_add_i32 s23, s55, s41
	ds_read_b128 v[180:183], v147 offset:16384
	ds_read_b128 v[184:187], v147 offset:17408
	ds_read_b128 v[188:191], v147 offset:18432
	ds_read_b128 v[192:195], v147 offset:19456
	ds_read_b128 v[196:199], v147 offset:20480
	ds_read_b128 v[200:203], v147 offset:21504
	ds_read_b128 v[204:207], v147 offset:22528
	ds_read_b128 v[208:211], v147 offset:23552
	s_waitcnt vmcnt(2)
	s_waitcnt lgkmcnt(0)
	s_barrier
	s_setprio 1
	s_waitcnt lgkmcnt(0)
	v_mfma_f32_16x16x32_bf16 v[64:67], v[148:151], v[180:183], v[64:67]
	v_mfma_f32_16x16x32_bf16 v[60:63], v[156:159], v[180:183], v[60:63]
	v_mfma_f32_16x16x32_bf16 v[48:51], v[148:151], v[188:191], v[48:51]
	v_mfma_f32_16x16x32_bf16 v[44:47], v[156:159], v[188:191], v[44:47]
	s_mov_b32 m0, s23
	s_nop 0
	global_load_lds_dwordx4 v136, s[28:29]
	v_mfma_f32_16x16x32_bf16 v[32:35], v[148:151], v[196:199], v[32:35]
	v_mfma_f32_16x16x32_bf16 v[28:31], v[156:159], v[196:199], v[28:31]
	v_mfma_f32_16x16x32_bf16 v[16:19], v[148:151], v[204:207], v[16:19]
	v_mfma_f32_16x16x32_bf16 v[12:15], v[156:159], v[204:207], v[12:15]
	s_add_i32 m0, s23, 0x2000
	s_mov_b64 s[100:101], s[28:29]
	global_load_lds_dwordx4 v132, s[28:29]
	v_mfma_f32_16x16x32_bf16 v[64:67], v[152:155], v[184:187], v[64:67]
	v_mfma_f32_16x16x32_bf16 v[60:63], v[160:163], v[184:187], v[60:63]
	v_mfma_f32_16x16x32_bf16 v[48:51], v[152:155], v[192:195], v[48:51]
	v_mfma_f32_16x16x32_bf16 v[44:47], v[160:163], v[192:195], v[44:47]
	s_add_u32 s28, s28, s2
	s_addc_u32 s29, s29, s3
	s_add_i32 s21, s21, s41
	s_mov_b32 m0, s21
	s_nop 0
	global_load_lds_dwordx4 v136, s[28:29]
	v_mfma_f32_16x16x32_bf16 v[32:35], v[152:155], v[200:203], v[32:35]
	v_mfma_f32_16x16x32_bf16 v[28:31], v[160:163], v[200:203], v[28:31]
	v_mfma_f32_16x16x32_bf16 v[16:19], v[152:155], v[208:211], v[16:19]
	v_mfma_f32_16x16x32_bf16 v[12:15], v[160:163], v[208:211], v[12:15]
	s_add_i32 m0, s21, 0x2000
	s_nop 0
	global_load_lds_dwordx4 v132, s[28:29]
	s_setprio 0
	s_setprio 1
	v_mfma_f32_16x16x32_bf16 v[56:59], v[164:167], v[180:183], v[56:59]
	v_mfma_f32_16x16x32_bf16 v[52:55], v[172:175], v[180:183], v[52:55]
	v_mfma_f32_16x16x32_bf16 v[40:43], v[164:167], v[188:191], v[40:43]
	v_mfma_f32_16x16x32_bf16 v[36:39], v[172:175], v[188:191], v[36:39]
	s_mov_b32 m0, s42
	s_nop 0
	global_load_lds_dwordx4 v138, s[30:31]
	v_mfma_f32_16x16x32_bf16 v[24:27], v[164:167], v[196:199], v[24:27]
	v_mfma_f32_16x16x32_bf16 v[20:23], v[172:175], v[196:199], v[20:23]
	v_mfma_f32_16x16x32_bf16 v[8:11], v[164:167], v[204:207], v[8:11]
	v_mfma_f32_16x16x32_bf16 v[4:7], v[172:175], v[204:207], v[4:7]
	s_mov_b32 m0, s43
	s_nop 0
	global_load_lds_dwordx4 v134, s[30:31]
	v_mfma_f32_16x16x32_bf16 v[56:59], v[168:171], v[184:187], v[56:59]
	v_mfma_f32_16x16x32_bf16 v[52:55], v[176:179], v[184:187], v[52:55]
	v_mfma_f32_16x16x32_bf16 v[40:43], v[168:171], v[192:195], v[40:43]
	v_mfma_f32_16x16x32_bf16 v[36:39], v[176:179], v[192:195], v[36:39]
	v_mfma_f32_16x16x32_bf16 v[24:27], v[168:171], v[200:203], v[24:27]
	v_mfma_f32_16x16x32_bf16 v[20:23], v[176:179], v[200:203], v[20:23]
	v_mfma_f32_16x16x32_bf16 v[8:11], v[168:171], v[208:211], v[8:11]
	v_mfma_f32_16x16x32_bf16 v[4:7], v[176:179], v[208:211], v[4:7]
	s_setprio 0
	s_barrier
	s_add_i32 s21, 0, 0x18000
	s_add_i32 s23, 0, 0x1c000
	ds_read_b128 v[148:151], v226 offset:32768
	ds_read_b128 v[152:155], v226 offset:33792
	ds_read_b128 v[156:159], v226 offset:34816
	ds_read_b128 v[160:163], v226 offset:35840
	ds_read_b128 v[164:167], v226 offset:49152
	ds_read_b128 v[168:171], v226 offset:50176
	ds_read_b128 v[172:175], v226 offset:51200
	ds_read_b128 v[176:179], v226 offset:52224
	s_add_u32 s28, s30, s2
	s_addc_u32 s29, s31, s3
	ds_read_b128 v[180:183], v147 offset:32768
	ds_read_b128 v[184:187], v147 offset:33792
	ds_read_b128 v[188:191], v147 offset:34816
	ds_read_b128 v[192:195], v147 offset:35840
	ds_read_b128 v[196:199], v147 offset:36864
	ds_read_b128 v[200:203], v147 offset:37888
	ds_read_b128 v[204:207], v147 offset:38912
	ds_read_b128 v[208:211], v147 offset:39936
	s_waitcnt vmcnt(6)
	s_waitcnt lgkmcnt(0)
	s_barrier
	s_setprio 1
	s_waitcnt lgkmcnt(0)
	v_mfma_f32_16x16x32_bf16 v[124:127], v[148:151], v[180:183], v[124:127]
	v_mfma_f32_16x16x32_bf16 v[128:131], v[156:159], v[180:183], v[128:131]
	v_mfma_f32_16x16x32_bf16 v[112:115], v[148:151], v[188:191], v[112:115]
	v_mfma_f32_16x16x32_bf16 v[108:111], v[156:159], v[188:191], v[108:111]
	s_mov_b32 m0, s44
	s_nop 0
	global_load_lds_dwordx4 v138, s[28:29]
	v_mfma_f32_16x16x32_bf16 v[96:99], v[148:151], v[196:199], v[96:99]
	v_mfma_f32_16x16x32_bf16 v[92:95], v[156:159], v[196:199], v[92:95]
	v_mfma_f32_16x16x32_bf16 v[80:83], v[148:151], v[204:207], v[80:83]
	v_mfma_f32_16x16x32_bf16 v[76:79], v[156:159], v[204:207], v[76:79]
	s_mov_b32 m0, s45
	s_nop 0
	global_load_lds_dwordx4 v134, s[28:29]
	v_mfma_f32_16x16x32_bf16 v[124:127], v[152:155], v[184:187], v[124:127]
	v_mfma_f32_16x16x32_bf16 v[128:131], v[160:163], v[184:187], v[128:131]
	v_mfma_f32_16x16x32_bf16 v[112:115], v[152:155], v[192:195], v[112:115]
	v_mfma_f32_16x16x32_bf16 v[108:111], v[160:163], v[192:195], v[108:111]
	v_mfma_f32_16x16x32_bf16 v[96:99], v[152:155], v[200:203], v[96:99]
	v_mfma_f32_16x16x32_bf16 v[92:95], v[160:163], v[200:203], v[92:95]
	v_mfma_f32_16x16x32_bf16 v[80:83], v[152:155], v[208:211], v[80:83]
	v_mfma_f32_16x16x32_bf16 v[76:79], v[160:163], v[208:211], v[76:79]
	s_setprio 0
	s_setprio 1
	v_mfma_f32_16x16x32_bf16 v[120:123], v[164:167], v[180:183], v[120:123]
	v_mfma_f32_16x16x32_bf16 v[116:119], v[172:175], v[180:183], v[116:119]
	v_mfma_f32_16x16x32_bf16 v[104:107], v[164:167], v[188:191], v[104:107]
	v_mfma_f32_16x16x32_bf16 v[100:103], v[172:175], v[188:191], v[100:103]
	v_mfma_f32_16x16x32_bf16 v[88:91], v[164:167], v[196:199], v[88:91]
	v_mfma_f32_16x16x32_bf16 v[84:87], v[172:175], v[196:199], v[84:87]
	v_mfma_f32_16x16x32_bf16 v[72:75], v[164:167], v[204:207], v[72:75]
	v_mfma_f32_16x16x32_bf16 v[68:71], v[172:175], v[204:207], v[68:71]
	v_mfma_f32_16x16x32_bf16 v[120:123], v[168:171], v[184:187], v[120:123]
	v_mfma_f32_16x16x32_bf16 v[116:119], v[176:179], v[184:187], v[116:119]
	v_mfma_f32_16x16x32_bf16 v[104:107], v[168:171], v[192:195], v[104:107]
	v_mfma_f32_16x16x32_bf16 v[100:103], v[176:179], v[192:195], v[100:103]
	v_mfma_f32_16x16x32_bf16 v[88:91], v[168:171], v[200:203], v[88:91]
	v_mfma_f32_16x16x32_bf16 v[84:87], v[176:179], v[200:203], v[84:87]
	v_mfma_f32_16x16x32_bf16 v[72:75], v[168:171], v[208:211], v[72:75]
	v_mfma_f32_16x16x32_bf16 v[68:71], v[176:179], v[208:211], v[68:71]
	s_setprio 0
	s_barrier
	s_add_i32 s21, s21, s41
	s_add_u32 s98, s100, s24
	s_addc_u32 s99, s101, s25
	ds_read_b128 v[180:183], v147 offset:49152
	ds_read_b128 v[184:187], v147 offset:50176
	ds_read_b128 v[188:191], v147 offset:51200
	ds_read_b128 v[192:195], v147 offset:52224
	ds_read_b128 v[196:199], v147 offset:53248
	ds_read_b128 v[200:203], v147 offset:54272
	ds_read_b128 v[204:207], v147 offset:55296
	ds_read_b128 v[208:211], v147 offset:56320
	s_waitcnt vmcnt(2)
	s_waitcnt lgkmcnt(0)
	s_barrier
	s_setprio 1
	s_waitcnt lgkmcnt(0)
	v_mfma_f32_16x16x32_bf16 v[64:67], v[148:151], v[180:183], v[64:67]
	v_mfma_f32_16x16x32_bf16 v[60:63], v[156:159], v[180:183], v[60:63]
	v_mfma_f32_16x16x32_bf16 v[48:51], v[148:151], v[188:191], v[48:51]
	v_mfma_f32_16x16x32_bf16 v[44:47], v[156:159], v[188:191], v[44:47]
	s_mov_b32 m0, s21
	s_nop 0
	global_load_lds_dwordx4 v136, s[98:99]
	v_mfma_f32_16x16x32_bf16 v[32:35], v[148:151], v[196:199], v[32:35]
	v_mfma_f32_16x16x32_bf16 v[28:31], v[156:159], v[196:199], v[28:31]
	v_mfma_f32_16x16x32_bf16 v[16:19], v[148:151], v[204:207], v[16:19]
	v_mfma_f32_16x16x32_bf16 v[12:15], v[156:159], v[204:207], v[12:15]
	s_add_i32 m0, s21, 0x2000
	s_add_i32 s21, s23, s41
	global_load_lds_dwordx4 v132, s[98:99]
	v_mfma_f32_16x16x32_bf16 v[64:67], v[152:155], v[184:187], v[64:67]
	v_mfma_f32_16x16x32_bf16 v[60:63], v[160:163], v[184:187], v[60:63]
	v_mfma_f32_16x16x32_bf16 v[48:51], v[152:155], v[192:195], v[48:51]
	v_mfma_f32_16x16x32_bf16 v[44:47], v[160:163], v[192:195], v[44:47]
	s_add_u32 s98, s98, s2
	s_addc_u32 s99, s99, s3
	s_mov_b32 m0, s21
	s_nop 0
	global_load_lds_dwordx4 v136, s[98:99]
	v_mfma_f32_16x16x32_bf16 v[32:35], v[152:155], v[200:203], v[32:35]
	v_mfma_f32_16x16x32_bf16 v[28:31], v[160:163], v[200:203], v[28:31]
	v_mfma_f32_16x16x32_bf16 v[16:19], v[152:155], v[208:211], v[16:19]
	v_mfma_f32_16x16x32_bf16 v[12:15], v[160:163], v[208:211], v[12:15]
	s_add_i32 m0, s21, 0x2000
	s_nop 0
	global_load_lds_dwordx4 v132, s[98:99]
	s_setprio 0
	s_setprio 1
	v_mfma_f32_16x16x32_bf16 v[56:59], v[164:167], v[180:183], v[56:59]
	v_mfma_f32_16x16x32_bf16 v[52:55], v[172:175], v[180:183], v[52:55]
	v_mfma_f32_16x16x32_bf16 v[40:43], v[164:167], v[188:191], v[40:43]
	v_mfma_f32_16x16x32_bf16 v[36:39], v[172:175], v[188:191], v[36:39]
	s_add_u32 s98, s30, s24
	s_addc_u32 s99, s31, s25
	s_mov_b32 m0, s47
	s_nop 0
	global_load_lds_dwordx4 v138, s[98:99]
	v_mfma_f32_16x16x32_bf16 v[24:27], v[164:167], v[196:199], v[24:27]
	v_mfma_f32_16x16x32_bf16 v[20:23], v[172:175], v[196:199], v[20:23]
	v_mfma_f32_16x16x32_bf16 v[8:11], v[164:167], v[204:207], v[8:11]
	v_mfma_f32_16x16x32_bf16 v[4:7], v[172:175], v[204:207], v[4:7]
	s_mov_b32 m0, s48
	s_nop 0
	global_load_lds_dwordx4 v134, s[98:99]
	v_mfma_f32_16x16x32_bf16 v[56:59], v[168:171], v[184:187], v[56:59]
	v_mfma_f32_16x16x32_bf16 v[52:55], v[176:179], v[184:187], v[52:55]
	v_mfma_f32_16x16x32_bf16 v[40:43], v[168:171], v[192:195], v[40:43]
	v_mfma_f32_16x16x32_bf16 v[36:39], v[176:179], v[192:195], v[36:39]
	v_mfma_f32_16x16x32_bf16 v[24:27], v[168:171], v[200:203], v[24:27]
	v_mfma_f32_16x16x32_bf16 v[20:23], v[176:179], v[200:203], v[20:23]
	v_mfma_f32_16x16x32_bf16 v[8:11], v[168:171], v[208:211], v[8:11]
	v_mfma_f32_16x16x32_bf16 v[4:7], v[176:179], v[208:211], v[4:7]
	s_setprio 0
	s_barrier
	s_add_u32 s26, s26, 0x100
	s_addc_u32 s27, s27, 0
	s_add_u32 s19, s19, 0x100
	s_addc_u32 s20, s20, 0
	s_cmp_ge_i32 s22, s46
	s_mov_b32 s21, s22
	s_cbranch_scc0 .LBB0_3499

	.amdhsa_kernel _Z3fwd4Args
		.amdhsa_group_segment_fixed_size 0
		.amdhsa_private_segment_fixed_size 0
		.amdhsa_kernarg_size 472
		.amdhsa_user_sgpr_count 2
		.amdhsa_user_sgpr_dispatch_ptr 0
		.amdhsa_user_sgpr_queue_ptr 0
		.amdhsa_user_sgpr_kernarg_segment_ptr 1
		.amdhsa_user_sgpr_dispatch_id 0
		.amdhsa_user_sgpr_kernarg_preload_length 0
		.amdhsa_user_sgpr_kernarg_preload_offset 0
		.amdhsa_user_sgpr_private_segment_size 0
		.amdhsa_uses_dynamic_stack 0
		.amdhsa_enable_private_segment 0
		.amdhsa_system_sgpr_workgroup_id_x 1
		.amdhsa_system_sgpr_workgroup_id_y 0
		.amdhsa_system_sgpr_workgroup_id_z 0
		.amdhsa_system_sgpr_workgroup_info 0
		.amdhsa_system_vgpr_workitem_id 0
		.amdhsa_next_free_vgpr 256
		.amdhsa_next_free_sgpr 102
		.amdhsa_accum_offset 256
		.amdhsa_reserve_vcc 1
		.amdhsa_float_round_mode_32 0
		.amdhsa_float_round_mode_16_64 0
		.amdhsa_float_denorm_mode_32 3
		.amdhsa_float_denorm_mode_16_64 3
		.amdhsa_dx10_clamp 1
		.amdhsa_ieee_mode 1
		.amdhsa_fp16_overflow 0
		.amdhsa_tg_split 0
		.amdhsa_exception_fp_ieee_invalid_op 0
		.amdhsa_exception_fp_denorm_src 0
		.amdhsa_exception_fp_ieee_div_zero 0
		.amdhsa_exception_fp_ieee_overflow 0
		.amdhsa_exception_fp_ieee_underflow 0
		.amdhsa_exception_fp_ieee_inexact 0
		.amdhsa_exception_int_div_zero 0
	.end_amdhsa_kernel

amdhsa.kernels:
  - .agpr_count:     0
    .args:
      - .offset:         0
        .size:           216
        .value_kind:     by_value
      - .offset:         216
        .size:           4
        .value_kind:     hidden_block_count_x
      - .offset:         220
        .size:           4
        .value_kind:     hidden_block_count_y
      - .offset:         224
        .size:           4
        .value_kind:     hidden_block_count_z
      - .offset:         228
        .size:           2
        .value_kind:     hidden_group_size_x
      - .offset:         230
        .size:           2
        .value_kind:     hidden_group_size_y
      - .offset:         232
        .size:           2
        .value_kind:     hidden_group_size_z
      - .offset:         234
        .size:           2
        .value_kind:     hidden_remainder_x
      - .offset:         236
        .size:           2
        .value_kind:     hidden_remainder_y
      - .offset:         238
        .size:           2
        .value_kind:     hidden_remainder_z
      - .offset:         256
        .size:           8
        .value_kind:     hidden_global_offset_x
      - .offset:         264
        .size:           8
        .value_kind:     hidden_global_offset_y
      - .offset:         272
        .size:           8
        .value_kind:     hidden_global_offset_z
      - .offset:         280
        .size:           2
        .value_kind:     hidden_grid_dims
      - .offset:         336
        .size:           4
        .value_kind:     hidden_dynamic_lds_size
    .group_segment_fixed_size: 0
    .kernarg_segment_align: 8
    .kernarg_segment_size: 472
    .language:       OpenCL C
    .language_version:
      - 2
      - 0
    .max_flat_workgroup_size: 512
    .name:           _Z3fwd4Args
    .private_segment_fixed_size: 0
    .sgpr_count:     108
    .sgpr_spill_count: 243
    .symbol:         _Z3fwd4Args.kd
    .uniform_work_group_size: 1
    .uses_dynamic_stack: false
    .vgpr_count:     256
    .vgpr_spill_count: 0
    .wavefront_size: 64
